# P6 slot scatter: the 4-trip load->LDS->store loop becomes one straight block with all 12 loads issued first (on top of the attention prologue overlap)
# baseline (speedup 1.0000x reference)
.Lp6_scatter:
	s_mov_b64 s[98:99], 0x1000
	s_mov_b64 s[100:101], 0x400000
	global_load_dword v140, v[8:9], off
	v_lshl_add_u64 v[132:133], v[8:9], 0, s[100:101]
	v_lshl_add_u64 v[130:131], v[8:9], 0, s[98:99]
	s_mov_b64 s[100:101], 0x200000
	v_lshl_add_u64 v[136:137], v[8:9], 0, s[100:101]
	global_load_dword v144, v[132:133], off
	global_load_dword v148, v[136:137], off
	global_load_dword v141, v[8:9], off offset:2048
	global_load_dword v145, v[132:133], off offset:2048
	global_load_dword v149, v[136:137], off offset:2048
	v_lshl_add_u64 v[134:135], v[132:133], 0, s[98:99]
	v_lshl_add_u64 v[138:139], v[136:137], 0, s[98:99]
	global_load_dword v142, v[130:131], off
	global_load_dword v146, v[134:135], off
	global_load_dword v150, v[138:139], off
	global_load_dword v143, v[130:131], off offset:2048
	global_load_dword v147, v[134:135], off offset:2048
	global_load_dword v151, v[138:139], off offset:2048
	s_waitcnt vmcnt(9)
	v_lshl_add_u32 v154, v140, 2, 0
	v_add_u32_e32 v155, 0x20800, v154
	v_add_u32_e32 v154, 0x20400, v154
	ds_read_b32 v155, v155
	ds_read_b32 v154, v154
	v_add_u32_e32 v152, s1, v10
	v_lshrrev_b32_e32 v153, 3, v152
	s_waitcnt lgkmcnt(0)
	v_add3_u32 v154, v154, v155, v144
	v_ashrrev_i32_e32 v155, 31, v154
	v_lshlrev_b64 v[156:157], 2, v[154:155]
	v_lshl_add_u64 v[158:159], s[12:13], 0, v[156:157]
	v_lshl_add_u64 v[160:161], s[10:11], 0, v[156:157]
	v_lshl_add_u64 v[156:157], s[8:9], 0, v[156:157]
	global_store_dword v[158:159], v153, off
	global_store_dword v[160:161], v152, off
	global_store_dword v[156:157], v148, off
	global_store_dword v[132:133], v154, off
	s_waitcnt vmcnt(10)
	v_lshl_add_u32 v154, v141, 2, 0
	v_add_u32_e32 v155, 0x20800, v154
	v_add_u32_e32 v154, 0x20400, v154
	ds_read_b32 v155, v155
	ds_read_b32 v154, v154
	v_add_u32_e32 v152, s1, v10
	v_add_u32_e32 v152, 0x200, v152
	v_lshrrev_b32_e32 v153, 3, v152
	s_waitcnt lgkmcnt(0)
	v_add3_u32 v154, v154, v155, v145
	v_ashrrev_i32_e32 v155, 31, v154
	v_lshlrev_b64 v[156:157], 2, v[154:155]
	v_lshl_add_u64 v[158:159], s[12:13], 0, v[156:157]
	v_lshl_add_u64 v[160:161], s[10:11], 0, v[156:157]
	v_lshl_add_u64 v[156:157], s[8:9], 0, v[156:157]
	global_store_dword v[158:159], v153, off
	global_store_dword v[160:161], v152, off
	global_store_dword v[156:157], v149, off
	global_store_dword v[132:133], v154, off offset:2048
	s_waitcnt vmcnt(11)
	v_lshl_add_u32 v154, v142, 2, 0
	v_add_u32_e32 v155, 0x20800, v154
	v_add_u32_e32 v154, 0x20400, v154
	ds_read_b32 v155, v155
	ds_read_b32 v154, v154
	v_add_u32_e32 v152, s1, v10
	v_add_u32_e32 v152, 0x400, v152
	v_lshrrev_b32_e32 v153, 3, v152
	s_waitcnt lgkmcnt(0)
	v_add3_u32 v154, v154, v155, v146
	v_ashrrev_i32_e32 v155, 31, v154
	v_lshlrev_b64 v[156:157], 2, v[154:155]
	v_lshl_add_u64 v[158:159], s[12:13], 0, v[156:157]
	v_lshl_add_u64 v[160:161], s[10:11], 0, v[156:157]
	v_lshl_add_u64 v[156:157], s[8:9], 0, v[156:157]
	global_store_dword v[158:159], v153, off
	global_store_dword v[160:161], v152, off
	global_store_dword v[156:157], v150, off
	global_store_dword v[134:135], v154, off
	s_waitcnt vmcnt(12)
	v_lshl_add_u32 v154, v143, 2, 0
	v_add_u32_e32 v155, 0x20800, v154
	v_add_u32_e32 v154, 0x20400, v154
	ds_read_b32 v155, v155
	ds_read_b32 v154, v154
	v_add_u32_e32 v152, s1, v10
	v_add_u32_e32 v152, 0x600, v152
	v_lshrrev_b32_e32 v153, 3, v152
	s_waitcnt lgkmcnt(0)
	v_add3_u32 v154, v154, v155, v147
	v_ashrrev_i32_e32 v155, 31, v154
	v_lshlrev_b64 v[156:157], 2, v[154:155]
	v_lshl_add_u64 v[158:159], s[12:13], 0, v[156:157]
	v_lshl_add_u64 v[160:161], s[10:11], 0, v[156:157]
	v_lshl_add_u64 v[156:157], s[8:9], 0, v[156:157]
	global_store_dword v[158:159], v153, off
	global_store_dword v[160:161], v152, off
	global_store_dword v[156:157], v151, off
	global_store_dword v[134:135], v154, off offset:2048
	s_branch .LBB0_1003
